# baseline (speedup 1.0000x reference)
.LBB2_2:
	s_or_b64 exec, exec, s[4:5]
	s_movk_i32 s2, 0x2a0
	v_cmp_gt_u32_e64 s[2:3], s2, v0
	v_mov_b32_e32 v7, 0
	v_mov_b32_e32 v8, 0
	v_mov_b32_e32 v9, 0
	s_and_saveexec_b64 s[4:5], s[2:3]
	s_cbranch_execz .LBB2_4
	v_add_co_u32_e32 v2, vcc, 0xd000, v68
	s_nop 1
	v_addc_co_u32_e32 v3, vcc, 0, v69, vcc
	global_load_dwordx4 v[6:9], v[2:3], off
.LBB2_4:
	s_or_b64 exec, exec, s[4:5]
	s_movk_i32 s4, 0x1a0
	v_cmp_gt_u32_e64 s[4:5], s4, v0
	v_mov_b32_e32 v2, 0
	v_mov_b32_e32 v10, 0
	v_mov_b32_e32 v11, 0
	v_mov_b32_e32 v12, 0
	v_mov_b32_e32 v13, 0
	s_and_saveexec_b64 s[6:7], s[4:5]
	s_cbranch_execz .LBB2_6
	v_add_co_u32_e32 v4, vcc, 0xe000, v68
	s_nop 1
	v_addc_co_u32_e32 v5, vcc, 0, v69, vcc
	global_load_dwordx4 v[10:13], v[4:5], off

.LBB2_8:
	s_or_b64 exec, exec, s[12:13]
	s_waitcnt vmcnt(1)
	v_cvt_f32_f16_e32 v124, v62
	v_cvt_f32_f16_sdwa v126, v62 dst_sel:DWORD dst_unused:UNUSED_PAD src0_sel:WORD_1
	v_cvt_f32_f16_e32 v132, v63
	v_cvt_f32_f16_sdwa v133, v63 dst_sel:DWORD dst_unused:UNUSED_PAD src0_sel:WORD_1
	v_cvt_f32_f16_e32 v129, v64
	v_cvt_f32_f16_sdwa v131, v64 dst_sel:DWORD dst_unused:UNUSED_PAD src0_sel:WORD_1
	v_cvt_f32_f16_e32 v134, v65
	v_cvt_f32_f16_sdwa v135, v65 dst_sel:DWORD dst_unused:UNUSED_PAD src0_sel:WORD_1
	s_mov_b32 s12, 0xff7fffff
	v_cvt_f32_f16_e32 v117, v58
	v_cvt_f32_f16_sdwa v120, v58 dst_sel:DWORD dst_unused:UNUSED_PAD src0_sel:WORD_1
	v_cvt_f32_f16_e32 v121, v60
	v_cvt_f32_f16_sdwa v123, v60 dst_sel:DWORD dst_unused:UNUSED_PAD src0_sel:WORD_1
	v_cvt_f32_f16_e32 v109, v54
	v_cvt_f32_f16_sdwa v112, v54 dst_sel:DWORD dst_unused:UNUSED_PAD src0_sel:WORD_1
	v_cvt_f32_f16_e32 v116, v55
	v_cvt_f32_f16_sdwa v118, v55 dst_sel:DWORD dst_unused:UNUSED_PAD src0_sel:WORD_1
	v_cvt_f32_f16_e32 v113, v56
	v_cvt_f32_f16_sdwa v115, v56 dst_sel:DWORD dst_unused:UNUSED_PAD src0_sel:WORD_1
	v_cvt_f32_f16_e32 v119, v57
	v_cvt_f32_f16_sdwa v122, v57 dst_sel:DWORD dst_unused:UNUSED_PAD src0_sel:WORD_1
	v_cvt_f32_f16_e32 v101, v50
	v_cvt_f32_f16_sdwa v104, v50 dst_sel:DWORD dst_unused:UNUSED_PAD src0_sel:WORD_1
	v_cvt_f32_f16_e32 v108, v51
	v_cvt_f32_f16_sdwa v110, v51 dst_sel:DWORD dst_unused:UNUSED_PAD src0_sel:WORD_1
	v_cvt_f32_f16_e32 v105, v52
	v_cvt_f32_f16_sdwa v107, v52 dst_sel:DWORD dst_unused:UNUSED_PAD src0_sel:WORD_1
	v_cvt_f32_f16_e32 v111, v53
	v_cvt_f32_f16_sdwa v114, v53 dst_sel:DWORD dst_unused:UNUSED_PAD src0_sel:WORD_1
	v_cvt_f32_f16_e32 v93, v46
	v_cvt_f32_f16_sdwa v96, v46 dst_sel:DWORD dst_unused:UNUSED_PAD src0_sel:WORD_1
	v_cvt_f32_f16_e32 v100, v47
	v_cvt_f32_f16_sdwa v102, v47 dst_sel:DWORD dst_unused:UNUSED_PAD src0_sel:WORD_1
	v_cvt_f32_f16_e32 v97, v48
	v_cvt_f32_f16_sdwa v99, v48 dst_sel:DWORD dst_unused:UNUSED_PAD src0_sel:WORD_1
	v_cvt_f32_f16_e32 v103, v49
	v_cvt_f32_f16_sdwa v106, v49 dst_sel:DWORD dst_unused:UNUSED_PAD src0_sel:WORD_1
	v_cvt_f32_f16_e32 v85, v42
	v_cvt_f32_f16_sdwa v88, v42 dst_sel:DWORD dst_unused:UNUSED_PAD src0_sel:WORD_1
	v_cvt_f32_f16_e32 v92, v43
	v_cvt_f32_f16_sdwa v94, v43 dst_sel:DWORD dst_unused:UNUSED_PAD src0_sel:WORD_1
	v_cvt_f32_f16_e32 v89, v44
	v_cvt_f32_f16_sdwa v91, v44 dst_sel:DWORD dst_unused:UNUSED_PAD src0_sel:WORD_1
	v_cvt_f32_f16_e32 v95, v45
	v_cvt_f32_f16_sdwa v98, v45 dst_sel:DWORD dst_unused:UNUSED_PAD src0_sel:WORD_1
	v_cvt_f32_f16_e32 v63, v38
	v_cvt_f32_f16_sdwa v72, v38 dst_sel:DWORD dst_unused:UNUSED_PAD src0_sel:WORD_1
	v_cvt_f32_f16_e32 v80, v39
	v_cvt_f32_f16_sdwa v86, v39 dst_sel:DWORD dst_unused:UNUSED_PAD src0_sel:WORD_1
	v_cvt_f32_f16_e32 v73, v40
	v_cvt_f32_f16_sdwa v79, v40 dst_sel:DWORD dst_unused:UNUSED_PAD src0_sel:WORD_1
	v_cvt_f32_f16_e32 v87, v41
	v_cvt_f32_f16_sdwa v90, v41 dst_sel:DWORD dst_unused:UNUSED_PAD src0_sel:WORD_1
	v_cvt_f32_f16_e32 v51, v34
	v_cvt_f32_f16_sdwa v54, v34 dst_sel:DWORD dst_unused:UNUSED_PAD src0_sel:WORD_1
	v_cvt_f32_f16_e32 v60, v35
	v_cvt_f32_f16_sdwa v64, v35 dst_sel:DWORD dst_unused:UNUSED_PAD src0_sel:WORD_1
	v_cvt_f32_f16_e32 v55, v36
	v_cvt_f32_f16_sdwa v57, v36 dst_sel:DWORD dst_unused:UNUSED_PAD src0_sel:WORD_1
	v_cvt_f32_f16_e32 v65, v37
	v_cvt_f32_f16_sdwa v74, v37 dst_sel:DWORD dst_unused:UNUSED_PAD src0_sel:WORD_1
	v_cvt_f32_f16_e32 v43, v30
	v_cvt_f32_f16_sdwa v46, v30 dst_sel:DWORD dst_unused:UNUSED_PAD src0_sel:WORD_1
	v_cvt_f32_f16_e32 v50, v31
	v_cvt_f32_f16_sdwa v52, v31 dst_sel:DWORD dst_unused:UNUSED_PAD src0_sel:WORD_1
	v_cvt_f32_f16_e32 v47, v32
	v_cvt_f32_f16_sdwa v49, v32 dst_sel:DWORD dst_unused:UNUSED_PAD src0_sel:WORD_1
	v_cvt_f32_f16_e32 v53, v33
	v_cvt_f32_f16_sdwa v56, v33 dst_sel:DWORD dst_unused:UNUSED_PAD src0_sel:WORD_1
	v_cvt_f32_f16_e32 v35, v26
	v_cvt_f32_f16_sdwa v38, v26 dst_sel:DWORD dst_unused:UNUSED_PAD src0_sel:WORD_1
	v_cvt_f32_f16_e32 v42, v27
	v_cvt_f32_f16_sdwa v44, v27 dst_sel:DWORD dst_unused:UNUSED_PAD src0_sel:WORD_1
	v_cvt_f32_f16_e32 v39, v28
	v_cvt_f32_f16_sdwa v41, v28 dst_sel:DWORD dst_unused:UNUSED_PAD src0_sel:WORD_1
	v_cvt_f32_f16_e32 v45, v29
	v_cvt_f32_f16_sdwa v48, v29 dst_sel:DWORD dst_unused:UNUSED_PAD src0_sel:WORD_1
	v_cvt_f32_f16_e32 v27, v22
	v_cvt_f32_f16_sdwa v30, v22 dst_sel:DWORD dst_unused:UNUSED_PAD src0_sel:WORD_1
	v_cvt_f32_f16_e32 v34, v23
	v_cvt_f32_f16_sdwa v36, v23 dst_sel:DWORD dst_unused:UNUSED_PAD src0_sel:WORD_1
	v_cvt_f32_f16_e32 v31, v24
	v_cvt_f32_f16_sdwa v33, v24 dst_sel:DWORD dst_unused:UNUSED_PAD src0_sel:WORD_1
	v_cvt_f32_f16_e32 v37, v25
	v_cvt_f32_f16_sdwa v40, v25 dst_sel:DWORD dst_unused:UNUSED_PAD src0_sel:WORD_1
	s_waitcnt vmcnt(0)
	v_mov_b32_e32 v67, v6
	v_cvt_f32_f16_e32 v22, v18
	v_cvt_f32_f16_sdwa v23, v18 dst_sel:DWORD dst_unused:UNUSED_PAD src0_sel:WORD_1
	v_cvt_f32_f16_e32 v26, v19
	v_cvt_f32_f16_sdwa v28, v19 dst_sel:DWORD dst_unused:UNUSED_PAD src0_sel:WORD_1
	v_cvt_f32_f16_e32 v24, v20
	v_cvt_f32_f16_sdwa v25, v20 dst_sel:DWORD dst_unused:UNUSED_PAD src0_sel:WORD_1
	v_cvt_f32_f16_e32 v29, v21
	v_cvt_f32_f16_sdwa v32, v21 dst_sel:DWORD dst_unused:UNUSED_PAD src0_sel:WORD_1
	v_cvt_f32_f16_e32 v18, v14
	v_cvt_f32_f16_sdwa v6, v14 dst_sel:DWORD dst_unused:UNUSED_PAD src0_sel:WORD_1
	v_cvt_f32_f16_e32 v20, v15
	v_cvt_f32_f16_sdwa v19, v15 dst_sel:DWORD dst_unused:UNUSED_PAD src0_sel:WORD_1
	v_cvt_f32_f16_e32 v15, v16
	v_cvt_f32_f16_sdwa v14, v16 dst_sel:DWORD dst_unused:UNUSED_PAD src0_sel:WORD_1
	v_cvt_f32_f16_e32 v21, v17
	v_cvt_f32_f16_sdwa v16, v17 dst_sel:DWORD dst_unused:UNUSED_PAD src0_sel:WORD_1
	v_max3_f32 v17, v124, s12, v126
	v_cvt_f32_f16_e32 v125, v59
	v_cvt_f32_f16_sdwa v127, v59 dst_sel:DWORD dst_unused:UNUSED_PAD src0_sel:WORD_1
	v_max3_f32 v17, v17, v132, v133
	v_max3_f32 v17, v17, v129, v131
	v_cvt_f32_f16_e32 v128, v61
	v_cvt_f32_f16_sdwa v130, v61 dst_sel:DWORD dst_unused:UNUSED_PAD src0_sel:WORD_1
	v_max3_f32 v17, v17, v134, v135
	v_max3_f32 v17, v17, v117, v120
	v_max3_f32 v17, v17, v125, v127
	v_max3_f32 v17, v17, v121, v123
	v_max3_f32 v17, v17, v128, v130
	v_max3_f32 v17, v17, v109, v112
	v_max3_f32 v17, v17, v116, v118
	v_max3_f32 v17, v17, v113, v115
	v_max3_f32 v17, v17, v119, v122
	v_max3_f32 v17, v17, v101, v104
	v_max3_f32 v17, v17, v108, v110
	v_max3_f32 v17, v17, v105, v107
	v_max3_f32 v17, v17, v111, v114
	v_max3_f32 v17, v17, v93, v96
	v_max3_f32 v17, v17, v100, v102
	v_max3_f32 v17, v17, v97, v99
	v_max3_f32 v17, v17, v103, v106
	v_max3_f32 v17, v17, v85, v88
	v_max3_f32 v17, v17, v92, v94
	v_max3_f32 v17, v17, v89, v91
	v_max3_f32 v17, v17, v95, v98
	v_max3_f32 v17, v17, v63, v72
	v_max3_f32 v17, v17, v80, v86
	v_max3_f32 v17, v17, v73, v79
	v_max3_f32 v17, v17, v87, v90
	v_max3_f32 v17, v17, v51, v54
	v_max3_f32 v17, v17, v60, v64
	v_max3_f32 v17, v17, v55, v57
	v_max3_f32 v17, v17, v65, v74
	v_max3_f32 v17, v17, v43, v46
	v_max3_f32 v17, v17, v50, v52
	v_max3_f32 v17, v17, v47, v49
	v_max3_f32 v17, v17, v53, v56
	v_max3_f32 v17, v17, v35, v38
	v_max3_f32 v17, v17, v42, v44
	v_max3_f32 v17, v17, v39, v41
	v_max3_f32 v17, v17, v45, v48
	v_max3_f32 v17, v17, v27, v30
	v_max3_f32 v17, v17, v34, v36
	v_max3_f32 v17, v17, v31, v33
	v_max3_f32 v17, v17, v37, v40
	v_max3_f32 v17, v17, v22, v23
	v_max3_f32 v17, v17, v26, v28
	v_max3_f32 v17, v17, v24, v25
	s_movk_i32 s12, 0x3a0
	v_max3_f32 v136, v17, v29, v32
	v_cmp_gt_u32_e32 vcc, s12, v0
	s_and_saveexec_b64 s[12:13], vcc
	v_max3_f32 v17, v136, v18, v6
	v_max3_f32 v17, v17, v20, v19
	v_max3_f32 v17, v17, v15, v14
	v_max3_f32 v136, v17, v21, v16
	s_or_b64 exec, exec, s[12:13]
	v_cvt_f32_f16_e32 v77, v67
	v_cvt_f32_f16_sdwa v75, v67 dst_sel:DWORD dst_unused:UNUSED_PAD src0_sel:WORD_1
	v_cvt_f32_f16_e32 v83, v7
	v_cvt_f32_f16_sdwa v81, v7 dst_sel:DWORD dst_unused:UNUSED_PAD src0_sel:WORD_1
	v_cvt_f32_f16_e32 v78, v8
	v_cvt_f32_f16_sdwa v76, v8 dst_sel:DWORD dst_unused:UNUSED_PAD src0_sel:WORD_1
	v_cvt_f32_f16_e32 v84, v9
	v_cvt_f32_f16_sdwa v82, v9 dst_sel:DWORD dst_unused:UNUSED_PAD src0_sel:WORD_1
	s_and_saveexec_b64 s[12:13], s[2:3]
	v_max3_f32 v7, v136, v77, v75
	v_max3_f32 v7, v7, v83, v81
	v_max3_f32 v7, v7, v78, v76
	v_max3_f32 v136, v7, v84, v82
	s_or_b64 exec, exec, s[12:13]
	v_cvt_f32_f16_e32 v61, v10
	v_cvt_f32_f16_sdwa v58, v10 dst_sel:DWORD dst_unused:UNUSED_PAD src0_sel:WORD_1
	v_cvt_f32_f16_e32 v68, v11
	v_cvt_f32_f16_sdwa v66, v11 dst_sel:DWORD dst_unused:UNUSED_PAD src0_sel:WORD_1
	v_cvt_f32_f16_e32 v62, v12
	v_cvt_f32_f16_sdwa v59, v12 dst_sel:DWORD dst_unused:UNUSED_PAD src0_sel:WORD_1
	v_cvt_f32_f16_e32 v69, v13
	v_cvt_f32_f16_sdwa v67, v13 dst_sel:DWORD dst_unused:UNUSED_PAD src0_sel:WORD_1
	s_and_saveexec_b64 s[12:13], s[4:5]
	v_max3_f32 v7, v136, v61, v58
	v_max3_f32 v7, v7, v68, v66
	v_max3_f32 v7, v7, v62, v59
	v_max3_f32 v136, v7, v69, v67
	s_or_b64 exec, exec, s[12:13]
	v_cvt_f32_f16_e32 v9, v2
	v_cvt_f32_f16_sdwa v7, v2 dst_sel:DWORD dst_unused:UNUSED_PAD src0_sel:WORD_1
	v_cvt_f32_f16_e32 v13, v3
	v_cvt_f32_f16_sdwa v11, v3 dst_sel:DWORD dst_unused:UNUSED_PAD src0_sel:WORD_1
	v_cvt_f32_f16_e32 v10, v4
	v_cvt_f32_f16_sdwa v8, v4 dst_sel:DWORD dst_unused:UNUSED_PAD src0_sel:WORD_1
	v_cvt_f32_f16_e32 v17, v5
	v_cvt_f32_f16_sdwa v12, v5 dst_sel:DWORD dst_unused:UNUSED_PAD src0_sel:WORD_1
	s_and_saveexec_b64 s[12:13], s[6:7]
	v_max3_f32 v2, v136, v9, v7
	v_max3_f32 v2, v2, v13, v11
	v_max3_f32 v2, v2, v10, v8
	v_max3_f32 v136, v2, v17, v12
	s_or_b64 exec, exec, s[12:13]
	v_sub_f32_e32 v2, v124, v136
	v_mul_f32_e32 v2, 0x3fb8aa3b, v2
	v_sub_f32_e32 v3, v126, v136
	v_exp_f32_e32 v2, v2
	v_mul_f32_e32 v3, 0x3fb8aa3b, v3
	v_sub_f32_e32 v4, v132, v136
	v_exp_f32_e32 v3, v3
	v_mul_f32_e32 v4, 0x3fb8aa3b, v4
	v_sub_f32_e32 v5, v133, v136
	v_exp_f32_e32 v4, v4
	v_mul_f32_e32 v5, 0x3fb8aa3b, v5
	v_exp_f32_e32 v5, v5
	v_add_f32_e32 v2, 0, v2
	v_add_f32_e32 v2, v2, v3
	v_sub_f32_e32 v3, v129, v136
	v_add_f32_e32 v2, v2, v4
	v_mul_f32_e32 v3, 0x3fb8aa3b, v3
	v_sub_f32_e32 v4, v131, v136
	v_add_f32_e32 v2, v2, v5
	v_exp_f32_e32 v3, v3
	v_mul_f32_e32 v4, 0x3fb8aa3b, v4
	v_sub_f32_e32 v5, v134, v136
	v_exp_f32_e32 v4, v4
	v_mul_f32_e32 v5, 0x3fb8aa3b, v5
	v_sub_f32_e32 v137, v135, v136
	v_exp_f32_e32 v5, v5
	v_mul_f32_e32 v137, 0x3fb8aa3b, v137
	v_exp_f32_e32 v137, v137
	v_add_f32_e32 v2, v2, v3
	v_sub_f32_e32 v3, v117, v136
	v_add_f32_e32 v2, v2, v4
	v_mul_f32_e32 v3, 0x3fb8aa3b, v3
	v_sub_f32_e32 v4, v120, v136
	v_add_f32_e32 v2, v2, v5
	v_exp_f32_e32 v3, v3
	v_mul_f32_e32 v4, 0x3fb8aa3b, v4
	v_sub_f32_e32 v5, v125, v136
	v_add_f32_e32 v2, v2, v137
	v_exp_f32_e32 v4, v4
	v_mul_f32_e32 v5, 0x3fb8aa3b, v5
	v_sub_f32_e32 v137, v127, v136
	v_exp_f32_e32 v5, v5
	v_mul_f32_e32 v137, 0x3fb8aa3b, v137
	v_exp_f32_e32 v137, v137
	v_add_f32_e32 v2, v2, v3
	v_sub_f32_e32 v3, v121, v136
	v_add_f32_e32 v2, v2, v4
	v_mul_f32_e32 v3, 0x3fb8aa3b, v3
	v_sub_f32_e32 v4, v123, v136
	v_add_f32_e32 v2, v2, v5
	v_exp_f32_e32 v3, v3
	v_mul_f32_e32 v4, 0x3fb8aa3b, v4
	v_sub_f32_e32 v5, v128, v136
	v_add_f32_e32 v2, v2, v137
	v_exp_f32_e32 v4, v4
	v_mul_f32_e32 v5, 0x3fb8aa3b, v5
	v_sub_f32_e32 v137, v130, v136
	v_exp_f32_e32 v5, v5
	v_mul_f32_e32 v137, 0x3fb8aa3b, v137
	v_exp_f32_e32 v137, v137
	v_add_f32_e32 v2, v2, v3
	v_sub_f32_e32 v3, v109, v136
	v_add_f32_e32 v2, v2, v4
	v_mul_f32_e32 v3, 0x3fb8aa3b, v3
	v_sub_f32_e32 v4, v112, v136
	v_add_f32_e32 v2, v2, v5
	v_exp_f32_e32 v3, v3
	v_mul_f32_e32 v4, 0x3fb8aa3b, v4
	v_sub_f32_e32 v5, v116, v136
	v_add_f32_e32 v2, v2, v137
	v_exp_f32_e32 v4, v4
	v_mul_f32_e32 v5, 0x3fb8aa3b, v5
	v_sub_f32_e32 v137, v118, v136
	v_exp_f32_e32 v5, v5
	v_mul_f32_e32 v137, 0x3fb8aa3b, v137
	v_exp_f32_e32 v137, v137
	v_add_f32_e32 v2, v2, v3
	v_sub_f32_e32 v3, v113, v136
	v_add_f32_e32 v2, v2, v4
	v_mul_f32_e32 v3, 0x3fb8aa3b, v3
	v_sub_f32_e32 v4, v115, v136
	v_add_f32_e32 v2, v2, v5
	v_exp_f32_e32 v3, v3
	v_mul_f32_e32 v4, 0x3fb8aa3b, v4
	v_sub_f32_e32 v5, v119, v136
	v_add_f32_e32 v2, v2, v137
	v_exp_f32_e32 v4, v4
	v_mul_f32_e32 v5, 0x3fb8aa3b, v5
	v_sub_f32_e32 v137, v122, v136
	v_exp_f32_e32 v5, v5
	v_mul_f32_e32 v137, 0x3fb8aa3b, v137
	v_exp_f32_e32 v137, v137
	v_add_f32_e32 v2, v2, v3
	v_sub_f32_e32 v3, v101, v136
	v_add_f32_e32 v2, v2, v4
	v_mul_f32_e32 v3, 0x3fb8aa3b, v3
	v_sub_f32_e32 v4, v104, v136
	v_add_f32_e32 v2, v2, v5
	v_exp_f32_e32 v3, v3
	v_mul_f32_e32 v4, 0x3fb8aa3b, v4
	v_sub_f32_e32 v5, v108, v136
	v_add_f32_e32 v2, v2, v137
	v_exp_f32_e32 v4, v4
	v_mul_f32_e32 v5, 0x3fb8aa3b, v5
	v_sub_f32_e32 v137, v110, v136
	v_exp_f32_e32 v5, v5
	v_mul_f32_e32 v137, 0x3fb8aa3b, v137
	v_exp_f32_e32 v137, v137
	v_add_f32_e32 v2, v2, v3
	v_sub_f32_e32 v3, v105, v136
	v_add_f32_e32 v2, v2, v4
	v_mul_f32_e32 v3, 0x3fb8aa3b, v3
	v_sub_f32_e32 v4, v107, v136
	v_add_f32_e32 v2, v2, v5
	v_exp_f32_e32 v3, v3
	v_mul_f32_e32 v4, 0x3fb8aa3b, v4
	v_sub_f32_e32 v5, v111, v136
	v_add_f32_e32 v2, v2, v137
	v_exp_f32_e32 v4, v4
	v_mul_f32_e32 v5, 0x3fb8aa3b, v5
	v_sub_f32_e32 v137, v114, v136
	v_exp_f32_e32 v5, v5
	v_mul_f32_e32 v137, 0x3fb8aa3b, v137
	v_exp_f32_e32 v137, v137
	v_add_f32_e32 v2, v2, v3
	v_sub_f32_e32 v3, v93, v136
	v_add_f32_e32 v2, v2, v4
	v_mul_f32_e32 v3, 0x3fb8aa3b, v3
	v_sub_f32_e32 v4, v96, v136
	v_add_f32_e32 v2, v2, v5
	v_exp_f32_e32 v3, v3
	v_mul_f32_e32 v4, 0x3fb8aa3b, v4
	v_sub_f32_e32 v5, v100, v136
	v_add_f32_e32 v2, v2, v137
	v_exp_f32_e32 v4, v4
	v_mul_f32_e32 v5, 0x3fb8aa3b, v5
	v_sub_f32_e32 v137, v102, v136
	v_exp_f32_e32 v5, v5
	v_mul_f32_e32 v137, 0x3fb8aa3b, v137
	v_exp_f32_e32 v137, v137
	v_add_f32_e32 v2, v2, v3
	v_sub_f32_e32 v3, v97, v136
	v_add_f32_e32 v2, v2, v4
	v_mul_f32_e32 v3, 0x3fb8aa3b, v3
	v_sub_f32_e32 v4, v99, v136
	v_add_f32_e32 v2, v2, v5
	v_exp_f32_e32 v3, v3
	v_mul_f32_e32 v4, 0x3fb8aa3b, v4
	v_sub_f32_e32 v5, v103, v136
	v_add_f32_e32 v2, v2, v137
	v_exp_f32_e32 v4, v4
	v_mul_f32_e32 v5, 0x3fb8aa3b, v5
	v_sub_f32_e32 v137, v106, v136
	v_exp_f32_e32 v5, v5
	v_mul_f32_e32 v137, 0x3fb8aa3b, v137
	v_exp_f32_e32 v137, v137
	v_add_f32_e32 v2, v2, v3
	v_sub_f32_e32 v3, v85, v136
	v_add_f32_e32 v2, v2, v4
	v_mul_f32_e32 v3, 0x3fb8aa3b, v3
	v_sub_f32_e32 v4, v88, v136
	v_add_f32_e32 v2, v2, v5
	v_exp_f32_e32 v3, v3
	v_mul_f32_e32 v4, 0x3fb8aa3b, v4
	v_sub_f32_e32 v5, v92, v136
	v_add_f32_e32 v2, v2, v137
	v_exp_f32_e32 v4, v4
	v_mul_f32_e32 v5, 0x3fb8aa3b, v5
	v_sub_f32_e32 v137, v94, v136
	v_exp_f32_e32 v5, v5
	v_mul_f32_e32 v137, 0x3fb8aa3b, v137
	v_exp_f32_e32 v137, v137
	v_add_f32_e32 v2, v2, v3
	v_sub_f32_e32 v3, v89, v136
	v_add_f32_e32 v2, v2, v4
	v_mul_f32_e32 v3, 0x3fb8aa3b, v3
	v_sub_f32_e32 v4, v91, v136
	v_add_f32_e32 v2, v2, v5
	v_exp_f32_e32 v3, v3
	v_mul_f32_e32 v4, 0x3fb8aa3b, v4
	v_sub_f32_e32 v5, v95, v136
	v_add_f32_e32 v2, v2, v137
	v_exp_f32_e32 v4, v4
	v_mul_f32_e32 v5, 0x3fb8aa3b, v5
	v_sub_f32_e32 v137, v98, v136
	v_exp_f32_e32 v5, v5
	v_mul_f32_e32 v137, 0x3fb8aa3b, v137
	v_exp_f32_e32 v137, v137
	v_add_f32_e32 v2, v2, v3
	v_sub_f32_e32 v3, v63, v136
	v_add_f32_e32 v2, v2, v4
	v_mul_f32_e32 v3, 0x3fb8aa3b, v3
	v_sub_f32_e32 v4, v72, v136
	v_add_f32_e32 v2, v2, v5
	v_exp_f32_e32 v3, v3
	v_mul_f32_e32 v4, 0x3fb8aa3b, v4
	v_sub_f32_e32 v5, v80, v136
	v_add_f32_e32 v2, v2, v137
	v_exp_f32_e32 v4, v4
	v_mul_f32_e32 v5, 0x3fb8aa3b, v5
	v_sub_f32_e32 v137, v86, v136
	v_exp_f32_e32 v5, v5
	v_mul_f32_e32 v137, 0x3fb8aa3b, v137
	v_exp_f32_e32 v137, v137
	v_add_f32_e32 v2, v2, v3
	v_sub_f32_e32 v3, v73, v136
	v_add_f32_e32 v2, v2, v4
	v_mul_f32_e32 v3, 0x3fb8aa3b, v3
	v_sub_f32_e32 v4, v79, v136
	v_add_f32_e32 v2, v2, v5
	v_exp_f32_e32 v3, v3
	v_mul_f32_e32 v4, 0x3fb8aa3b, v4
	v_sub_f32_e32 v5, v87, v136
	v_add_f32_e32 v2, v2, v137
	v_exp_f32_e32 v4, v4
	v_mul_f32_e32 v5, 0x3fb8aa3b, v5
	v_sub_f32_e32 v137, v90, v136
	v_exp_f32_e32 v5, v5
	v_mul_f32_e32 v137, 0x3fb8aa3b, v137
	v_exp_f32_e32 v137, v137
	v_add_f32_e32 v2, v2, v3
	v_sub_f32_e32 v3, v51, v136
	v_add_f32_e32 v2, v2, v4
	v_mul_f32_e32 v3, 0x3fb8aa3b, v3
	v_sub_f32_e32 v4, v54, v136
	v_add_f32_e32 v2, v2, v5
	v_exp_f32_e32 v3, v3
	v_mul_f32_e32 v4, 0x3fb8aa3b, v4
	v_sub_f32_e32 v5, v60, v136
	v_add_f32_e32 v2, v2, v137
	v_exp_f32_e32 v4, v4
	v_mul_f32_e32 v5, 0x3fb8aa3b, v5
	v_sub_f32_e32 v137, v64, v136
	v_exp_f32_e32 v5, v5
	v_mul_f32_e32 v137, 0x3fb8aa3b, v137
	v_exp_f32_e32 v137, v137
	v_add_f32_e32 v2, v2, v3
	v_sub_f32_e32 v3, v55, v136
	v_add_f32_e32 v2, v2, v4
	v_mul_f32_e32 v3, 0x3fb8aa3b, v3
	v_sub_f32_e32 v4, v57, v136
	v_add_f32_e32 v2, v2, v5
	v_exp_f32_e32 v3, v3
	v_mul_f32_e32 v4, 0x3fb8aa3b, v4
	v_sub_f32_e32 v5, v65, v136
	v_add_f32_e32 v2, v2, v137
	v_exp_f32_e32 v4, v4
	v_mul_f32_e32 v5, 0x3fb8aa3b, v5
	v_sub_f32_e32 v137, v74, v136
	v_exp_f32_e32 v5, v5
	v_mul_f32_e32 v137, 0x3fb8aa3b, v137
	v_exp_f32_e32 v137, v137
	v_add_f32_e32 v2, v2, v3
	v_sub_f32_e32 v3, v43, v136
	v_add_f32_e32 v2, v2, v4
	v_mul_f32_e32 v3, 0x3fb8aa3b, v3
	v_sub_f32_e32 v4, v46, v136
	v_add_f32_e32 v2, v2, v5
	v_exp_f32_e32 v3, v3
	v_mul_f32_e32 v4, 0x3fb8aa3b, v4
	v_sub_f32_e32 v5, v50, v136
	v_add_f32_e32 v2, v2, v137
	v_exp_f32_e32 v4, v4
	v_mul_f32_e32 v5, 0x3fb8aa3b, v5
	v_sub_f32_e32 v137, v52, v136
	v_exp_f32_e32 v5, v5
	v_mul_f32_e32 v137, 0x3fb8aa3b, v137
	v_exp_f32_e32 v137, v137
	v_add_f32_e32 v2, v2, v3
	v_sub_f32_e32 v3, v47, v136
	v_add_f32_e32 v2, v2, v4
	v_mul_f32_e32 v3, 0x3fb8aa3b, v3
	v_sub_f32_e32 v4, v49, v136
	v_add_f32_e32 v2, v2, v5
	v_exp_f32_e32 v3, v3
	v_mul_f32_e32 v4, 0x3fb8aa3b, v4
	v_sub_f32_e32 v5, v53, v136
	v_add_f32_e32 v2, v2, v137
	v_exp_f32_e32 v4, v4
	v_mul_f32_e32 v5, 0x3fb8aa3b, v5
	v_sub_f32_e32 v137, v56, v136
	v_exp_f32_e32 v5, v5
	v_mul_f32_e32 v137, 0x3fb8aa3b, v137
	v_exp_f32_e32 v137, v137
	v_add_f32_e32 v2, v2, v3
	v_sub_f32_e32 v3, v35, v136
	v_add_f32_e32 v2, v2, v4
	v_mul_f32_e32 v3, 0x3fb8aa3b, v3
	v_sub_f32_e32 v4, v38, v136
	v_add_f32_e32 v2, v2, v5
	v_exp_f32_e32 v3, v3
	v_mul_f32_e32 v4, 0x3fb8aa3b, v4
	v_sub_f32_e32 v5, v42, v136
	v_add_f32_e32 v2, v2, v137
	v_exp_f32_e32 v4, v4
	v_mul_f32_e32 v5, 0x3fb8aa3b, v5
	v_sub_f32_e32 v137, v44, v136
	v_exp_f32_e32 v5, v5
	v_mul_f32_e32 v137, 0x3fb8aa3b, v137
	v_exp_f32_e32 v137, v137
	v_add_f32_e32 v2, v2, v3
	v_sub_f32_e32 v3, v39, v136
	v_add_f32_e32 v2, v2, v4
	v_mul_f32_e32 v3, 0x3fb8aa3b, v3
	v_sub_f32_e32 v4, v41, v136
	v_add_f32_e32 v2, v2, v5
	v_exp_f32_e32 v3, v3
	v_mul_f32_e32 v4, 0x3fb8aa3b, v4
	v_sub_f32_e32 v5, v45, v136
	v_add_f32_e32 v2, v2, v137
	v_exp_f32_e32 v4, v4
	v_mul_f32_e32 v5, 0x3fb8aa3b, v5
	v_sub_f32_e32 v137, v48, v136
	v_exp_f32_e32 v5, v5
	v_mul_f32_e32 v137, 0x3fb8aa3b, v137
	v_exp_f32_e32 v137, v137
	v_add_f32_e32 v2, v2, v3
	v_sub_f32_e32 v3, v27, v136
	v_add_f32_e32 v2, v2, v4
	v_mul_f32_e32 v3, 0x3fb8aa3b, v3
	v_sub_f32_e32 v4, v30, v136
	v_add_f32_e32 v2, v2, v5
	v_exp_f32_e32 v3, v3
	v_mul_f32_e32 v4, 0x3fb8aa3b, v4
	v_sub_f32_e32 v5, v34, v136
	v_add_f32_e32 v2, v2, v137
	v_exp_f32_e32 v4, v4
	v_mul_f32_e32 v5, 0x3fb8aa3b, v5
	v_sub_f32_e32 v137, v36, v136
	v_exp_f32_e32 v5, v5
	v_mul_f32_e32 v137, 0x3fb8aa3b, v137
	v_exp_f32_e32 v137, v137
	v_add_f32_e32 v2, v2, v3
	v_sub_f32_e32 v3, v31, v136
	v_add_f32_e32 v2, v2, v4
	v_mul_f32_e32 v3, 0x3fb8aa3b, v3
	v_sub_f32_e32 v4, v33, v136
	v_add_f32_e32 v2, v2, v5
	v_exp_f32_e32 v3, v3
	v_mul_f32_e32 v4, 0x3fb8aa3b, v4
	v_sub_f32_e32 v5, v37, v136
	v_add_f32_e32 v2, v2, v137
	v_exp_f32_e32 v4, v4
	v_mul_f32_e32 v5, 0x3fb8aa3b, v5
	v_sub_f32_e32 v137, v40, v136
	v_exp_f32_e32 v5, v5
	v_mul_f32_e32 v137, 0x3fb8aa3b, v137
	v_exp_f32_e32 v137, v137
	v_add_f32_e32 v2, v2, v3
	v_sub_f32_e32 v3, v22, v136
	v_add_f32_e32 v2, v2, v4
	v_mul_f32_e32 v3, 0x3fb8aa3b, v3
	v_sub_f32_e32 v4, v23, v136
	v_add_f32_e32 v2, v2, v5
	v_exp_f32_e32 v3, v3
	v_mul_f32_e32 v4, 0x3fb8aa3b, v4
	v_sub_f32_e32 v5, v26, v136
	v_add_f32_e32 v2, v2, v137
	v_exp_f32_e32 v4, v4
	v_mul_f32_e32 v5, 0x3fb8aa3b, v5
	v_sub_f32_e32 v137, v28, v136
	v_exp_f32_e32 v5, v5
	v_mul_f32_e32 v137, 0x3fb8aa3b, v137
	v_exp_f32_e32 v137, v137
	v_add_f32_e32 v2, v2, v3
	v_sub_f32_e32 v3, v24, v136
	v_add_f32_e32 v2, v2, v4
	v_mul_f32_e32 v3, 0x3fb8aa3b, v3
	v_sub_f32_e32 v4, v25, v136
	v_add_f32_e32 v2, v2, v5
	v_exp_f32_e32 v3, v3
	v_mul_f32_e32 v4, 0x3fb8aa3b, v4
	v_sub_f32_e32 v5, v29, v136
	v_add_f32_e32 v2, v2, v137
	v_exp_f32_e32 v4, v4
	v_mul_f32_e32 v5, 0x3fb8aa3b, v5
	v_sub_f32_e32 v137, v32, v136
	v_exp_f32_e32 v5, v5
	v_mul_f32_e32 v137, 0x3fb8aa3b, v137
	v_exp_f32_e32 v137, v137
	v_add_f32_e32 v2, v2, v3
	v_add_f32_e32 v2, v2, v4
	v_add_f32_e32 v2, v2, v5
	v_add_f32_e32 v2, v2, v137
	s_and_saveexec_b64 s[12:13], vcc
	s_cbranch_execnz .LBB2_28
	s_or_b64 exec, exec, s[12:13]
	s_and_saveexec_b64 s[12:13], s[2:3]
	s_cbranch_execnz .LBB2_29
